# DOWN epilogue rewritten by hand: paired waves swap 16-byte pieces through free LDS so every store covers whole 128-byte lines
# baseline (speedup 1.0000x reference)
.LBB0_843:
	v_and_b32_e32 v146, 15, v141
	v_bfe_u32 v147, v143, 4, 2
	v_bfe_u32 v148, v143, 6, 1
	v_lshrrev_b32_e32 v149, 3, v146
	v_xor_b32_e32 v149, v149, v148
	v_cmp_ne_u32_e64 s[66:67], 0, v149
	v_and_b32_e32 v150, 7, v146
	v_lshl_add_u32 v150, v150, 2, v147
	v_lshlrev_b32_e32 v150, 4, v150
	v_lshl_add_u32 v150, v148, 9, v150
	v_lshrrev_b32_e32 v151, 7, v143
	v_lshrrev_b32_e32 v156, 6, v141
	v_lshl_add_u32 v151, v156, 1, v151
	v_lshl_add_u32 v150, v151, 10, v150
	v_add_u32_e32 v150, 0x20000, v150
	v_xor_b32_e32 v151, 0x200, v150
	v_mov_b32_e32 v156, 0x3fc0
	v_sub_u32_e32 v157, 0, v156
	v_cmp_ne_u32_e32 vcc, 0, v148
	v_cndmask_b32_e32 v156, v157, v156, vcc
	v_cndmask_b32_e64 v156, 0, v156, s[66:67]
	v_lshl_add_u32 v152, s43, 8, v141
	v_lshl_add_u32 v157, s45, 8, v143
	v_lshl_add_u32 v152, v152, 11, v157
	v_add_u32_e32 v152, v152, v156
	v_mov_b32_e32 v153, 0
	v_lshl_add_u64 v[154:155], s[10:11], 0, v[152:153]
	v_med3_f32 v126, v126, s63, v230
	v_med3_f32 v127, v127, s63, v230
	v_med3_f32 v128, v128, s63, v230
	v_med3_f32 v129, v129, s63, v230
	v_cvt_pk_fp8_f32 v160, v126, v127
	v_cvt_pk_fp8_f32 v160, v128, v129 op_sel:[0,0,1]
	v_med3_f32 v122, v122, s63, v230
	v_med3_f32 v123, v123, s63, v230
	v_med3_f32 v124, v124, s63, v230
	v_med3_f32 v125, v125, s63, v230
	v_cvt_pk_fp8_f32 v161, v122, v123
	v_cvt_pk_fp8_f32 v161, v124, v125 op_sel:[0,0,1]
	v_med3_f32 v118, v118, s63, v230
	v_med3_f32 v119, v119, s63, v230
	v_med3_f32 v120, v120, s63, v230
	v_med3_f32 v121, v121, s63, v230
	v_cvt_pk_fp8_f32 v162, v118, v119
	v_cvt_pk_fp8_f32 v162, v120, v121 op_sel:[0,0,1]
	v_med3_f32 v114, v114, s63, v230
	v_med3_f32 v115, v115, s63, v230
	v_med3_f32 v116, v116, s63, v230
	v_med3_f32 v117, v117, s63, v230
	v_cvt_pk_fp8_f32 v163, v114, v115
	v_cvt_pk_fp8_f32 v163, v116, v117 op_sel:[0,0,1]
	s_mov_b64 exec, s[66:67]
	ds_write_b128 v150, v[160:163] offset:0
	s_mov_b64 exec, -1
	v_med3_f32 v110, v110, s63, v230
	v_med3_f32 v111, v111, s63, v230
	v_med3_f32 v112, v112, s63, v230
	v_med3_f32 v113, v113, s63, v230
	v_cvt_pk_fp8_f32 v164, v110, v111
	v_cvt_pk_fp8_f32 v164, v112, v113 op_sel:[0,0,1]
	v_med3_f32 v106, v106, s63, v230
	v_med3_f32 v107, v107, s63, v230
	v_med3_f32 v108, v108, s63, v230
	v_med3_f32 v109, v109, s63, v230
	v_cvt_pk_fp8_f32 v165, v106, v107
	v_cvt_pk_fp8_f32 v165, v108, v109 op_sel:[0,0,1]
	v_med3_f32 v102, v102, s63, v230
	v_med3_f32 v103, v103, s63, v230
	v_med3_f32 v104, v104, s63, v230
	v_med3_f32 v105, v105, s63, v230
	v_cvt_pk_fp8_f32 v166, v102, v103
	v_cvt_pk_fp8_f32 v166, v104, v105 op_sel:[0,0,1]
	v_med3_f32 v98, v98, s63, v230
	v_med3_f32 v99, v99, s63, v230
	v_med3_f32 v100, v100, s63, v230
	v_med3_f32 v101, v101, s63, v230
	v_cvt_pk_fp8_f32 v167, v98, v99
	v_cvt_pk_fp8_f32 v167, v100, v101 op_sel:[0,0,1]
	s_mov_b64 exec, s[66:67]
	ds_write_b128 v150, v[164:167] offset:4096
	s_mov_b64 exec, -1
	v_med3_f32 v94, v94, s63, v230
	v_med3_f32 v95, v95, s63, v230
	v_med3_f32 v96, v96, s63, v230
	v_med3_f32 v97, v97, s63, v230
	v_cvt_pk_fp8_f32 v168, v94, v95
	v_cvt_pk_fp8_f32 v168, v96, v97 op_sel:[0,0,1]
	v_med3_f32 v90, v90, s63, v230
	v_med3_f32 v91, v91, s63, v230
	v_med3_f32 v92, v92, s63, v230
	v_med3_f32 v93, v93, s63, v230
	v_cvt_pk_fp8_f32 v169, v90, v91
	v_cvt_pk_fp8_f32 v169, v92, v93 op_sel:[0,0,1]
	v_med3_f32 v86, v86, s63, v230
	v_med3_f32 v87, v87, s63, v230
	v_med3_f32 v88, v88, s63, v230
	v_med3_f32 v89, v89, s63, v230
	v_cvt_pk_fp8_f32 v170, v86, v87
	v_cvt_pk_fp8_f32 v170, v88, v89 op_sel:[0,0,1]
	v_med3_f32 v82, v82, s63, v230
	v_med3_f32 v83, v83, s63, v230
	v_med3_f32 v84, v84, s63, v230
	v_med3_f32 v85, v85, s63, v230
	v_cvt_pk_fp8_f32 v171, v82, v83
	v_cvt_pk_fp8_f32 v171, v84, v85 op_sel:[0,0,1]
	s_mov_b64 exec, s[66:67]
	ds_write_b128 v150, v[168:171] offset:8192
	s_mov_b64 exec, -1
	v_med3_f32 v78, v78, s63, v230
	v_med3_f32 v79, v79, s63, v230
	v_med3_f32 v80, v80, s63, v230
	v_med3_f32 v81, v81, s63, v230
	v_cvt_pk_fp8_f32 v172, v78, v79
	v_cvt_pk_fp8_f32 v172, v80, v81 op_sel:[0,0,1]
	v_med3_f32 v74, v74, s63, v230
	v_med3_f32 v75, v75, s63, v230
	v_med3_f32 v76, v76, s63, v230
	v_med3_f32 v77, v77, s63, v230
	v_cvt_pk_fp8_f32 v173, v74, v75
	v_cvt_pk_fp8_f32 v173, v76, v77 op_sel:[0,0,1]
	v_med3_f32 v70, v70, s63, v230
	v_med3_f32 v71, v71, s63, v230
	v_med3_f32 v72, v72, s63, v230
	v_med3_f32 v73, v73, s63, v230
	v_cvt_pk_fp8_f32 v174, v70, v71
	v_cvt_pk_fp8_f32 v174, v72, v73 op_sel:[0,0,1]
	v_med3_f32 v66, v66, s63, v230
	v_med3_f32 v67, v67, s63, v230
	v_med3_f32 v68, v68, s63, v230
	v_med3_f32 v69, v69, s63, v230
	v_cvt_pk_fp8_f32 v175, v66, v67
	v_cvt_pk_fp8_f32 v175, v68, v69 op_sel:[0,0,1]
	s_mov_b64 exec, s[66:67]
	ds_write_b128 v150, v[172:175] offset:12288
	s_mov_b64 exec, -1
	s_waitcnt lgkmcnt(0)
	s_barrier
	s_mov_b64 exec, s[66:67]
	ds_read_b128 v[160:163], v151 offset:0
	ds_read_b128 v[164:167], v151 offset:4096
	ds_read_b128 v[168:171], v151 offset:8192
	ds_read_b128 v[172:175], v151 offset:12288
	s_mov_b64 exec, -1
	v_med3_f32 v62, v62, s63, v230
	v_med3_f32 v63, v63, s63, v230
	v_med3_f32 v64, v64, s63, v230
	v_med3_f32 v65, v65, s63, v230
	v_cvt_pk_fp8_f32 v176, v62, v63
	v_cvt_pk_fp8_f32 v176, v64, v65 op_sel:[0,0,1]
	v_med3_f32 v58, v58, s63, v230
	v_med3_f32 v59, v59, s63, v230
	v_med3_f32 v60, v60, s63, v230
	v_med3_f32 v61, v61, s63, v230
	v_cvt_pk_fp8_f32 v177, v58, v59
	v_cvt_pk_fp8_f32 v177, v60, v61 op_sel:[0,0,1]
	v_med3_f32 v54, v54, s63, v230
	v_med3_f32 v55, v55, s63, v230
	v_med3_f32 v56, v56, s63, v230
	v_med3_f32 v57, v57, s63, v230
	v_cvt_pk_fp8_f32 v178, v54, v55
	v_cvt_pk_fp8_f32 v178, v56, v57 op_sel:[0,0,1]
	v_med3_f32 v50, v50, s63, v230
	v_med3_f32 v51, v51, s63, v230
	v_med3_f32 v52, v52, s63, v230
	v_med3_f32 v53, v53, s63, v230
	v_cvt_pk_fp8_f32 v179, v50, v51
	v_cvt_pk_fp8_f32 v179, v52, v53 op_sel:[0,0,1]
	v_med3_f32 v46, v46, s63, v230
	v_med3_f32 v47, v47, s63, v230
	v_med3_f32 v48, v48, s63, v230
	v_med3_f32 v49, v49, s63, v230
	v_cvt_pk_fp8_f32 v180, v46, v47
	v_cvt_pk_fp8_f32 v180, v48, v49 op_sel:[0,0,1]
	v_med3_f32 v42, v42, s63, v230
	v_med3_f32 v43, v43, s63, v230
	v_med3_f32 v44, v44, s63, v230
	v_med3_f32 v45, v45, s63, v230
	v_cvt_pk_fp8_f32 v181, v42, v43
	v_cvt_pk_fp8_f32 v181, v44, v45 op_sel:[0,0,1]
	v_med3_f32 v38, v38, s63, v230
	v_med3_f32 v39, v39, s63, v230
	v_med3_f32 v40, v40, s63, v230
	v_med3_f32 v41, v41, s63, v230
	v_cvt_pk_fp8_f32 v182, v38, v39
	v_cvt_pk_fp8_f32 v182, v40, v41 op_sel:[0,0,1]
	v_med3_f32 v34, v34, s63, v230
	v_med3_f32 v35, v35, s63, v230
	v_med3_f32 v36, v36, s63, v230
	v_med3_f32 v37, v37, s63, v230
	v_cvt_pk_fp8_f32 v183, v34, v35
	v_cvt_pk_fp8_f32 v183, v36, v37 op_sel:[0,0,1]
	v_med3_f32 v30, v30, s63, v230
	v_med3_f32 v31, v31, s63, v230
	v_med3_f32 v32, v32, s63, v230
	v_med3_f32 v33, v33, s63, v230
	v_cvt_pk_fp8_f32 v184, v30, v31
	v_cvt_pk_fp8_f32 v184, v32, v33 op_sel:[0,0,1]
	v_med3_f32 v26, v26, s63, v230
	v_med3_f32 v27, v27, s63, v230
	v_med3_f32 v28, v28, s63, v230
	v_med3_f32 v29, v29, s63, v230
	v_cvt_pk_fp8_f32 v185, v26, v27
	v_cvt_pk_fp8_f32 v185, v28, v29 op_sel:[0,0,1]
	v_med3_f32 v22, v22, s63, v230
	v_med3_f32 v23, v23, s63, v230
	v_med3_f32 v24, v24, s63, v230
	v_med3_f32 v25, v25, s63, v230
	v_cvt_pk_fp8_f32 v186, v22, v23
	v_cvt_pk_fp8_f32 v186, v24, v25 op_sel:[0,0,1]
	v_med3_f32 v18, v18, s63, v230
	v_med3_f32 v19, v19, s63, v230
	v_med3_f32 v20, v20, s63, v230
	v_med3_f32 v21, v21, s63, v230
	v_cvt_pk_fp8_f32 v187, v18, v19
	v_cvt_pk_fp8_f32 v187, v20, v21 op_sel:[0,0,1]
	v_med3_f32 v14, v14, s63, v230
	v_med3_f32 v15, v15, s63, v230
	v_med3_f32 v16, v16, s63, v230
	v_med3_f32 v17, v17, s63, v230
	v_cvt_pk_fp8_f32 v188, v14, v15
	v_cvt_pk_fp8_f32 v188, v16, v17 op_sel:[0,0,1]
	v_med3_f32 v10, v10, s63, v230
	v_med3_f32 v11, v11, s63, v230
	v_med3_f32 v12, v12, s63, v230
	v_med3_f32 v13, v13, s63, v230
	v_cvt_pk_fp8_f32 v189, v10, v11
	v_cvt_pk_fp8_f32 v189, v12, v13 op_sel:[0,0,1]
	v_med3_f32 v6, v6, s63, v230
	v_med3_f32 v7, v7, s63, v230
	v_med3_f32 v8, v8, s63, v230
	v_med3_f32 v9, v9, s63, v230
	v_cvt_pk_fp8_f32 v190, v6, v7
	v_cvt_pk_fp8_f32 v190, v8, v9 op_sel:[0,0,1]
	v_med3_f32 v2, v2, s63, v230
	v_med3_f32 v3, v3, s63, v230
	v_med3_f32 v4, v4, s63, v230
	v_med3_f32 v5, v5, s63, v230
	v_cvt_pk_fp8_f32 v191, v2, v3
	v_cvt_pk_fp8_f32 v191, v4, v5 op_sel:[0,0,1]
	s_waitcnt lgkmcnt(0)
	global_store_dwordx4 v[154:155], v[160:163], off
	v_add_co_u32_e32 v204, vcc, 0x8000, v154
	v_addc_co_u32_e32 v205, vcc, 0, v155, vcc
	global_store_dwordx4 v[204:205], v[164:167], off
	v_add_co_u32_e32 v206, vcc, 0x10000, v154
	v_addc_co_u32_e32 v207, vcc, 0, v155, vcc
	global_store_dwordx4 v[206:207], v[168:171], off
	v_add_co_u32_e32 v208, vcc, 0x18000, v154
	v_addc_co_u32_e32 v209, vcc, 0, v155, vcc
	global_store_dwordx4 v[208:209], v[172:175], off
	s_barrier
	s_mov_b64 exec, s[66:67]
	ds_write_b128 v150, v[176:179] offset:0
	s_mov_b64 exec, -1
	s_mov_b64 exec, s[66:67]
	ds_write_b128 v150, v[180:183] offset:4096
	s_mov_b64 exec, -1
	s_mov_b64 exec, s[66:67]
	ds_write_b128 v150, v[184:187] offset:8192
	s_mov_b64 exec, -1
	s_mov_b64 exec, s[66:67]
	ds_write_b128 v150, v[188:191] offset:12288
	s_mov_b64 exec, -1
	s_waitcnt lgkmcnt(0)
	s_barrier
	s_mov_b64 exec, s[66:67]
	ds_read_b128 v[176:179], v151 offset:0
	ds_read_b128 v[180:183], v151 offset:4096
	ds_read_b128 v[184:187], v151 offset:8192
	ds_read_b128 v[188:191], v151 offset:12288
	s_mov_b64 exec, -1
	s_waitcnt lgkmcnt(0)
	v_add_co_u32_e32 v202, vcc, 0x40000, v154
	v_addc_co_u32_e32 v203, vcc, 0, v155, vcc
	global_store_dwordx4 v[202:203], v[176:179], off
	v_add_co_u32_e32 v204, vcc, 0x48000, v154
	v_addc_co_u32_e32 v205, vcc, 0, v155, vcc
	global_store_dwordx4 v[204:205], v[180:183], off
	v_add_co_u32_e32 v206, vcc, 0x50000, v154
	v_addc_co_u32_e32 v207, vcc, 0, v155, vcc
	global_store_dwordx4 v[206:207], v[184:187], off
	v_add_co_u32_e32 v208, vcc, 0x58000, v154
	v_addc_co_u32_e32 v209, vcc, 0, v155, vcc
	global_store_dwordx4 v[208:209], v[188:191], off
	s_mov_b64 s[4:5], -1
	s_andn2_b64 vcc, exec, s[6:7]
	s_waitcnt vmcnt(8)
	s_cbranch_vccnz .LBB0_835
	s_andn2_b64 vcc, exec, s[12:13]
	s_cbranch_vccnz .LBB0_834
	s_barrier
	s_branch .LBB0_834
